# speedup vs baseline: 1.0168x; 1.0168x over previous
_Z8dog_mainPKfS0_S0_S0_S0_S0_S0_Pf:
	s_load_dwordx8 s[12:19], s[0:1], 0x0
	s_load_dwordx8 s[20:27], s[0:1], 0x20
	s_and_b32 s3, s2, 7
	s_lshl_b32 s3, s3, 5
	s_lshr_b32 s4, s2, 3
	s_add_i32 s4, s3, s4
	s_and_b32 s6, s4, 3
	s_lshr_b32 s7, s4, 2
	s_mov_b32 s5, 0
	s_lshl_b64 s[8:9], s[4:5], 18
	v_and_b32_e32 v1, 63, v0
	v_lshrrev_b32_e32 v2, 6, v0
	v_and_b32_e32 v3, 31, v0
	v_lshl_or_b32 v4, v2, 5, v3
	v_lshlrev_b32_e32 v5, 2, v4
	v_lshlrev_b32_e32 v6, 4, v1
	v_lshl_or_b32 v6, v2, 12, v6
	s_waitcnt lgkmcnt(0)
	global_load_dword v20, v5, s[18:19]
	global_load_dword v21, v5, s[20:21]
	global_load_dword v22, v5, s[22:23]
	global_load_dword v23, v5, s[24:25]
	global_load_dword v24, v5, s[14:15]
	global_load_dword v25, v5, s[16:17]
	s_add_u32 s12, s12, s8
	s_addc_u32 s13, s13, s9
	global_load_dwordx4 v[128:131], v6, s[12:13] offset:0 nt
	global_load_dwordx4 v[132:135], v6, s[12:13] offset:1024 nt
	global_load_dwordx4 v[136:139], v6, s[12:13] offset:2048 nt
	global_load_dwordx4 v[140:143], v6, s[12:13] offset:3072 nt
	v_add_u32_e32 v6, 0x8000, v6
	global_load_dwordx4 v[144:147], v6, s[12:13] offset:0 nt
	global_load_dwordx4 v[148:151], v6, s[12:13] offset:1024 nt
	global_load_dwordx4 v[152:155], v6, s[12:13] offset:2048 nt
	global_load_dwordx4 v[156:159], v6, s[12:13] offset:3072 nt
	v_bfe_u32 v7, v0, 5, 1
	v_and_b32_e32 v16, 1, v0
	v_cmp_eq_u32_e64 s[30:31], 0, v16
	v_and_b32_e32 v17, 2, v0
	v_cmp_eq_u32_e64 s[32:33], 0, v17
	v_and_b32_e32 v16, 3, v0
	v_lshrrev_b32_e32 v17, 2, v1
	v_lshlrev_b32_e32 v16, 5, v16
	v_lshl_add_u32 v16, v17, 1, v16
	v_lshrrev_b32_e32 v17, 1, v2
	s_movk_i32 s10, 0x110
	v_mad_u32_u24 v16, v17, s10, v16
	v_and_b32_e32 v17, 1, v2
	v_lshl_add_u32 v14, v17, 7, v16
	v_lshlrev_b32_e32 v17, 4, v7
	v_mad_u32_u24 v15, v3, s10, v17
	s_lshl_b32 s11, s6, 5
	v_lshl_add_u32 v18, v7, 2, s11
	v_cvt_f32_u32_e32 v18, v18
	v_lshlrev_b32_e32 v19, 3, v7
	v_cvt_f32_u32_e32 v19, v19
	s_waitcnt vmcnt(8)
	v_add_f32_e32 v26, v20, v21
	v_rcp_f32_e32 v27, v20
	v_rcp_f32_e32 v28, v26
	v_sub_f32_e32 v12, v19, v22
	v_sub_f32_e32 v13, v18, v23
	v_fma_f32 v29, -v20, v27, 1.0
	v_fma_f32 v30, -v26, v28, 1.0
	v_fma_f32 v27, v29, v27, v27
	v_fma_f32 v28, v30, v28, v28
	v_mul_f32_e32 v8, 0xbf38aa3b, v27
	v_mul_f32_e32 v9, 0xbf38aa3b, v28
	v_mul_f32_e32 v29, v24, v27
	v_mul_f32_e32 v30, v25, v28
	v_mul_f32_e32 v10, 0x3e22f983, v29
	v_mul_f32_e32 v11, 0x3e22f983, v30
	s_getpc_b64 s[44:45]
.Lpc_anchor:
	s_add_u32 s44, s44, _Z7dog_finPKfS0_Pf-.Lpc_anchor
	s_addc_u32 s45, s45, 0
	s_load_dwordx16 s[48:63], s[44:45], 0x0
	s_load_dwordx16 s[64:79], s[44:45], 0x40
	s_load_dwordx16 s[80:95], s[44:45], 0x80
	v_mul_f32_e32 v16, v12, v12
	v_add_f32_e32 v17, 0x3f800000, v12
	v_add_f32_e32 v18, 0x40000000, v12
	v_add_f32_e32 v19, 0x40400000, v12
	v_mul_f32_e32 v17, v17, v17
	v_mul_f32_e32 v18, v18, v18
	v_mul_f32_e32 v19, v19, v19
	v_mul_f32_e32 v20, v8, v16
	v_mul_f32_e32 v24, v9, v16
	v_mul_f32_e32 v21, v8, v17
	v_mul_f32_e32 v25, v9, v17
	v_mul_f32_e32 v22, v8, v18
	v_mul_f32_e32 v26, v9, v18
	v_mul_f32_e32 v23, v8, v19
	v_mul_f32_e32 v27, v9, v19
	v_exp_f32_e32 v20, v20
	v_exp_f32_e32 v21, v21
	v_exp_f32_e32 v22, v22
	v_exp_f32_e32 v23, v23
	v_exp_f32_e32 v24, v24
	v_exp_f32_e32 v25, v25
	v_exp_f32_e32 v26, v26
	v_exp_f32_e32 v27, v27
	v_cvt_pk_f16_f32 v32, v20, v21
	v_cvt_pk_f16_f32 v33, v22, v23
	v_cvt_pk_f16_f32 v64, v24, v25
	v_cvt_pk_f16_f32 v65, v26, v27
	v_add_f32_e32 v16, 0x40800000, v12
	v_add_f32_e32 v17, 0x40a00000, v12
	v_add_f32_e32 v18, 0x40c00000, v12
	v_add_f32_e32 v19, 0x40e00000, v12
	v_mul_f32_e32 v16, v16, v16
	v_mul_f32_e32 v17, v17, v17
	v_mul_f32_e32 v18, v18, v18
	v_mul_f32_e32 v19, v19, v19
	v_mul_f32_e32 v20, v8, v16
	v_mul_f32_e32 v24, v9, v16
	v_mul_f32_e32 v21, v8, v17
	v_mul_f32_e32 v25, v9, v17
	v_mul_f32_e32 v22, v8, v18
	v_mul_f32_e32 v26, v9, v18
	v_mul_f32_e32 v23, v8, v19
	v_mul_f32_e32 v27, v9, v19
	v_exp_f32_e32 v20, v20
	v_exp_f32_e32 v21, v21
	v_exp_f32_e32 v22, v22
	v_exp_f32_e32 v23, v23
	v_exp_f32_e32 v24, v24
	v_exp_f32_e32 v25, v25
	v_exp_f32_e32 v26, v26
	v_exp_f32_e32 v27, v27
	v_cvt_pk_f16_f32 v34, v20, v21
	v_cvt_pk_f16_f32 v35, v22, v23
	v_cvt_pk_f16_f32 v66, v24, v25
	v_cvt_pk_f16_f32 v67, v26, v27
	v_add_f32_e32 v16, 0x41800000, v12
	v_add_f32_e32 v17, 0x41880000, v12
	v_add_f32_e32 v18, 0x41900000, v12
	v_add_f32_e32 v19, 0x41980000, v12
	v_mul_f32_e32 v16, v16, v16
	v_mul_f32_e32 v17, v17, v17
	v_mul_f32_e32 v18, v18, v18
	v_mul_f32_e32 v19, v19, v19
	v_mul_f32_e32 v20, v8, v16
	v_mul_f32_e32 v24, v9, v16
	v_mul_f32_e32 v21, v8, v17
	v_mul_f32_e32 v25, v9, v17
	v_mul_f32_e32 v22, v8, v18
	v_mul_f32_e32 v26, v9, v18
	v_mul_f32_e32 v23, v8, v19
	v_mul_f32_e32 v27, v9, v19
	v_exp_f32_e32 v20, v20
	v_exp_f32_e32 v21, v21
	v_exp_f32_e32 v22, v22
	v_exp_f32_e32 v23, v23
	v_exp_f32_e32 v24, v24
	v_exp_f32_e32 v25, v25
	v_exp_f32_e32 v26, v26
	v_exp_f32_e32 v27, v27
	v_cvt_pk_f16_f32 v36, v20, v21
	v_cvt_pk_f16_f32 v37, v22, v23
	v_cvt_pk_f16_f32 v68, v24, v25
	v_cvt_pk_f16_f32 v69, v26, v27
	v_add_f32_e32 v16, 0x41a00000, v12
	v_add_f32_e32 v17, 0x41a80000, v12
	v_add_f32_e32 v18, 0x41b00000, v12
	v_add_f32_e32 v19, 0x41b80000, v12
	v_mul_f32_e32 v16, v16, v16
	v_mul_f32_e32 v17, v17, v17
	v_mul_f32_e32 v18, v18, v18
	v_mul_f32_e32 v19, v19, v19
	v_mul_f32_e32 v20, v8, v16
	v_mul_f32_e32 v24, v9, v16
	v_mul_f32_e32 v21, v8, v17
	v_mul_f32_e32 v25, v9, v17
	v_mul_f32_e32 v22, v8, v18
	v_mul_f32_e32 v26, v9, v18
	v_mul_f32_e32 v23, v8, v19
	v_mul_f32_e32 v27, v9, v19
	v_exp_f32_e32 v20, v20
	v_exp_f32_e32 v21, v21
	v_exp_f32_e32 v22, v22
	v_exp_f32_e32 v23, v23
	v_exp_f32_e32 v24, v24
	v_exp_f32_e32 v25, v25
	v_exp_f32_e32 v26, v26
	v_exp_f32_e32 v27, v27
	v_cvt_pk_f16_f32 v38, v20, v21
	v_cvt_pk_f16_f32 v39, v22, v23
	v_cvt_pk_f16_f32 v70, v24, v25
	v_cvt_pk_f16_f32 v71, v26, v27
	v_add_u32_e32 v6, 0x8000, v6
	global_load_dwordx4 v[160:163], v6, s[12:13] offset:0 nt
	global_load_dwordx4 v[164:167], v6, s[12:13] offset:1024 nt
	global_load_dwordx4 v[168:171], v6, s[12:13] offset:2048 nt
	global_load_dwordx4 v[172:175], v6, s[12:13] offset:3072 nt
	v_add_f32_e32 v16, 0x42000000, v12
	v_add_f32_e32 v17, 0x42040000, v12
	v_add_f32_e32 v18, 0x42080000, v12
	v_add_f32_e32 v19, 0x420c0000, v12
	v_mul_f32_e32 v16, v16, v16
	v_mul_f32_e32 v17, v17, v17
	v_mul_f32_e32 v18, v18, v18
	v_mul_f32_e32 v19, v19, v19
	v_mul_f32_e32 v20, v8, v16
	v_mul_f32_e32 v24, v9, v16
	v_mul_f32_e32 v21, v8, v17
	v_mul_f32_e32 v25, v9, v17
	v_mul_f32_e32 v22, v8, v18
	v_mul_f32_e32 v26, v9, v18
	v_mul_f32_e32 v23, v8, v19
	v_mul_f32_e32 v27, v9, v19
	v_exp_f32_e32 v20, v20
	v_exp_f32_e32 v21, v21
	v_exp_f32_e32 v22, v22
	v_exp_f32_e32 v23, v23
	v_exp_f32_e32 v24, v24
	v_exp_f32_e32 v25, v25
	v_exp_f32_e32 v26, v26
	v_exp_f32_e32 v27, v27
	v_cvt_pk_f16_f32 v40, v20, v21
	v_cvt_pk_f16_f32 v41, v22, v23
	v_cvt_pk_f16_f32 v72, v24, v25
	v_cvt_pk_f16_f32 v73, v26, v27
	v_add_f32_e32 v16, 0x42100000, v12
	v_add_f32_e32 v17, 0x42140000, v12
	v_add_f32_e32 v18, 0x42180000, v12
	v_add_f32_e32 v19, 0x421c0000, v12
	v_mul_f32_e32 v16, v16, v16
	v_mul_f32_e32 v17, v17, v17
	v_mul_f32_e32 v18, v18, v18
	v_mul_f32_e32 v19, v19, v19
	v_mul_f32_e32 v20, v8, v16
	v_mul_f32_e32 v24, v9, v16
	v_mul_f32_e32 v21, v8, v17
	v_mul_f32_e32 v25, v9, v17
	v_mul_f32_e32 v22, v8, v18
	v_mul_f32_e32 v26, v9, v18
	v_mul_f32_e32 v23, v8, v19
	v_mul_f32_e32 v27, v9, v19
	v_exp_f32_e32 v20, v20
	v_exp_f32_e32 v21, v21
	v_exp_f32_e32 v22, v22
	v_exp_f32_e32 v23, v23
	v_exp_f32_e32 v24, v24
	v_exp_f32_e32 v25, v25
	v_exp_f32_e32 v26, v26
	v_exp_f32_e32 v27, v27
	v_cvt_pk_f16_f32 v42, v20, v21
	v_cvt_pk_f16_f32 v43, v22, v23
	v_cvt_pk_f16_f32 v74, v24, v25
	v_cvt_pk_f16_f32 v75, v26, v27
	v_add_f32_e32 v16, 0x42400000, v12
	v_add_f32_e32 v17, 0x42440000, v12
	v_add_f32_e32 v18, 0x42480000, v12
	v_add_f32_e32 v19, 0x424c0000, v12
	v_mul_f32_e32 v16, v16, v16
	v_mul_f32_e32 v17, v17, v17
	v_mul_f32_e32 v18, v18, v18
	v_mul_f32_e32 v19, v19, v19
	v_mul_f32_e32 v20, v8, v16
	v_mul_f32_e32 v24, v9, v16
	v_mul_f32_e32 v21, v8, v17
	v_mul_f32_e32 v25, v9, v17
	v_mul_f32_e32 v22, v8, v18
	v_mul_f32_e32 v26, v9, v18
	v_mul_f32_e32 v23, v8, v19
	v_mul_f32_e32 v27, v9, v19
	v_exp_f32_e32 v20, v20
	v_exp_f32_e32 v21, v21
	v_exp_f32_e32 v22, v22
	v_exp_f32_e32 v23, v23
	v_exp_f32_e32 v24, v24
	v_exp_f32_e32 v25, v25
	v_exp_f32_e32 v26, v26
	v_exp_f32_e32 v27, v27
	v_cvt_pk_f16_f32 v44, v20, v21
	v_cvt_pk_f16_f32 v45, v22, v23
	v_cvt_pk_f16_f32 v76, v24, v25
	v_cvt_pk_f16_f32 v77, v26, v27
	v_add_f32_e32 v16, 0x42500000, v12
	v_add_f32_e32 v17, 0x42540000, v12
	v_add_f32_e32 v18, 0x42580000, v12
	v_add_f32_e32 v19, 0x425c0000, v12
	v_mul_f32_e32 v16, v16, v16
	v_mul_f32_e32 v17, v17, v17
	v_mul_f32_e32 v18, v18, v18
	v_mul_f32_e32 v19, v19, v19
	v_mul_f32_e32 v20, v8, v16
	v_mul_f32_e32 v24, v9, v16
	v_mul_f32_e32 v21, v8, v17
	v_mul_f32_e32 v25, v9, v17
	v_mul_f32_e32 v22, v8, v18
	v_mul_f32_e32 v26, v9, v18
	v_mul_f32_e32 v23, v8, v19
	v_mul_f32_e32 v27, v9, v19
	v_exp_f32_e32 v20, v20
	v_exp_f32_e32 v21, v21
	v_exp_f32_e32 v22, v22
	v_exp_f32_e32 v23, v23
	v_exp_f32_e32 v24, v24
	v_exp_f32_e32 v25, v25
	v_exp_f32_e32 v26, v26
	v_exp_f32_e32 v27, v27
	v_cvt_pk_f16_f32 v46, v20, v21
	v_cvt_pk_f16_f32 v47, v22, v23
	v_cvt_pk_f16_f32 v78, v24, v25
	v_cvt_pk_f16_f32 v79, v26, v27
	v_add_u32_e32 v6, 0x8000, v6
	global_load_dwordx4 v[176:179], v6, s[12:13] offset:0 nt
	global_load_dwordx4 v[180:183], v6, s[12:13] offset:1024 nt
	global_load_dwordx4 v[184:187], v6, s[12:13] offset:2048 nt
	global_load_dwordx4 v[188:191], v6, s[12:13] offset:3072 nt
	v_add_f32_e32 v16, 0x42800000, v12
	v_add_f32_e32 v17, 0x42820000, v12
	v_add_f32_e32 v18, 0x42840000, v12
	v_add_f32_e32 v19, 0x42860000, v12
	v_mul_f32_e32 v16, v16, v16
	v_mul_f32_e32 v17, v17, v17
	v_mul_f32_e32 v18, v18, v18
	v_mul_f32_e32 v19, v19, v19
	v_mul_f32_e32 v20, v8, v16
	v_mul_f32_e32 v24, v9, v16
	v_mul_f32_e32 v21, v8, v17
	v_mul_f32_e32 v25, v9, v17
	v_mul_f32_e32 v22, v8, v18
	v_mul_f32_e32 v26, v9, v18
	v_mul_f32_e32 v23, v8, v19
	v_mul_f32_e32 v27, v9, v19
	v_exp_f32_e32 v20, v20
	v_exp_f32_e32 v21, v21
	v_exp_f32_e32 v22, v22
	v_exp_f32_e32 v23, v23
	v_exp_f32_e32 v24, v24
	v_exp_f32_e32 v25, v25
	v_exp_f32_e32 v26, v26
	v_exp_f32_e32 v27, v27
	v_cvt_pk_f16_f32 v48, v20, v21
	v_cvt_pk_f16_f32 v49, v22, v23
	v_cvt_pk_f16_f32 v80, v24, v25
	v_cvt_pk_f16_f32 v81, v26, v27
	v_add_f32_e32 v16, 0x42880000, v12
	v_add_f32_e32 v17, 0x428a0000, v12
	v_add_f32_e32 v18, 0x428c0000, v12
	v_add_f32_e32 v19, 0x428e0000, v12
	v_mul_f32_e32 v16, v16, v16
	v_mul_f32_e32 v17, v17, v17
	v_mul_f32_e32 v18, v18, v18
	v_mul_f32_e32 v19, v19, v19
	v_mul_f32_e32 v20, v8, v16
	v_mul_f32_e32 v24, v9, v16
	v_mul_f32_e32 v21, v8, v17
	v_mul_f32_e32 v25, v9, v17
	v_mul_f32_e32 v22, v8, v18
	v_mul_f32_e32 v26, v9, v18
	v_mul_f32_e32 v23, v8, v19
	v_mul_f32_e32 v27, v9, v19
	v_exp_f32_e32 v20, v20
	v_exp_f32_e32 v21, v21
	v_exp_f32_e32 v22, v22
	v_exp_f32_e32 v23, v23
	v_exp_f32_e32 v24, v24
	v_exp_f32_e32 v25, v25
	v_exp_f32_e32 v26, v26
	v_exp_f32_e32 v27, v27
	v_cvt_pk_f16_f32 v50, v20, v21
	v_cvt_pk_f16_f32 v51, v22, v23
	v_cvt_pk_f16_f32 v82, v24, v25
	v_cvt_pk_f16_f32 v83, v26, v27
	v_add_f32_e32 v16, 0x42a00000, v12
	v_add_f32_e32 v17, 0x42a20000, v12
	v_add_f32_e32 v18, 0x42a40000, v12
	v_add_f32_e32 v19, 0x42a60000, v12
	v_mul_f32_e32 v16, v16, v16
	v_mul_f32_e32 v17, v17, v17
	v_mul_f32_e32 v18, v18, v18
	v_mul_f32_e32 v19, v19, v19
	v_mul_f32_e32 v20, v8, v16
	v_mul_f32_e32 v24, v9, v16
	v_mul_f32_e32 v21, v8, v17
	v_mul_f32_e32 v25, v9, v17
	v_mul_f32_e32 v22, v8, v18
	v_mul_f32_e32 v26, v9, v18
	v_mul_f32_e32 v23, v8, v19
	v_mul_f32_e32 v27, v9, v19
	v_exp_f32_e32 v20, v20
	v_exp_f32_e32 v21, v21
	v_exp_f32_e32 v22, v22
	v_exp_f32_e32 v23, v23
	v_exp_f32_e32 v24, v24
	v_exp_f32_e32 v25, v25
	v_exp_f32_e32 v26, v26
	v_exp_f32_e32 v27, v27
	v_cvt_pk_f16_f32 v52, v20, v21
	v_cvt_pk_f16_f32 v53, v22, v23
	v_cvt_pk_f16_f32 v84, v24, v25
	v_cvt_pk_f16_f32 v85, v26, v27
	v_add_f32_e32 v16, 0x42a80000, v12
	v_add_f32_e32 v17, 0x42aa0000, v12
	v_add_f32_e32 v18, 0x42ac0000, v12
	v_add_f32_e32 v19, 0x42ae0000, v12
	v_mul_f32_e32 v16, v16, v16
	v_mul_f32_e32 v17, v17, v17
	v_mul_f32_e32 v18, v18, v18
	v_mul_f32_e32 v19, v19, v19
	v_mul_f32_e32 v20, v8, v16
	v_mul_f32_e32 v24, v9, v16
	v_mul_f32_e32 v21, v8, v17
	v_mul_f32_e32 v25, v9, v17
	v_mul_f32_e32 v22, v8, v18
	v_mul_f32_e32 v26, v9, v18
	v_mul_f32_e32 v23, v8, v19
	v_mul_f32_e32 v27, v9, v19
	v_exp_f32_e32 v20, v20
	v_exp_f32_e32 v21, v21
	v_exp_f32_e32 v22, v22
	v_exp_f32_e32 v23, v23
	v_exp_f32_e32 v24, v24
	v_exp_f32_e32 v25, v25
	v_exp_f32_e32 v26, v26
	v_exp_f32_e32 v27, v27
	v_cvt_pk_f16_f32 v54, v20, v21
	v_cvt_pk_f16_f32 v55, v22, v23
	v_cvt_pk_f16_f32 v86, v24, v25
	v_cvt_pk_f16_f32 v87, v26, v27
	v_add_u32_e32 v6, 0x8000, v6
	global_load_dwordx4 v[192:195], v6, s[12:13] offset:0 nt
	global_load_dwordx4 v[196:199], v6, s[12:13] offset:1024 nt
	global_load_dwordx4 v[200:203], v6, s[12:13] offset:2048 nt
	global_load_dwordx4 v[204:207], v6, s[12:13] offset:3072 nt
	v_add_f32_e32 v16, 0x42c00000, v12
	v_add_f32_e32 v17, 0x42c20000, v12
	v_add_f32_e32 v18, 0x42c40000, v12
	v_add_f32_e32 v19, 0x42c60000, v12
	v_mul_f32_e32 v16, v16, v16
	v_mul_f32_e32 v17, v17, v17
	v_mul_f32_e32 v18, v18, v18
	v_mul_f32_e32 v19, v19, v19
	v_mul_f32_e32 v20, v8, v16
	v_mul_f32_e32 v24, v9, v16
	v_mul_f32_e32 v21, v8, v17
	v_mul_f32_e32 v25, v9, v17
	v_mul_f32_e32 v22, v8, v18
	v_mul_f32_e32 v26, v9, v18
	v_mul_f32_e32 v23, v8, v19
	v_mul_f32_e32 v27, v9, v19
	v_exp_f32_e32 v20, v20
	v_exp_f32_e32 v21, v21
	v_exp_f32_e32 v22, v22
	v_exp_f32_e32 v23, v23
	v_exp_f32_e32 v24, v24
	v_exp_f32_e32 v25, v25
	v_exp_f32_e32 v26, v26
	v_exp_f32_e32 v27, v27
	v_cvt_pk_f16_f32 v56, v20, v21
	v_cvt_pk_f16_f32 v57, v22, v23
	v_cvt_pk_f16_f32 v88, v24, v25
	v_cvt_pk_f16_f32 v89, v26, v27
	v_add_f32_e32 v16, 0x42c80000, v12
	v_add_f32_e32 v17, 0x42ca0000, v12
	v_add_f32_e32 v18, 0x42cc0000, v12
	v_add_f32_e32 v19, 0x42ce0000, v12
	v_mul_f32_e32 v16, v16, v16
	v_mul_f32_e32 v17, v17, v17
	v_mul_f32_e32 v18, v18, v18
	v_mul_f32_e32 v19, v19, v19
	v_mul_f32_e32 v20, v8, v16
	v_mul_f32_e32 v24, v9, v16
	v_mul_f32_e32 v21, v8, v17
	v_mul_f32_e32 v25, v9, v17
	v_mul_f32_e32 v22, v8, v18
	v_mul_f32_e32 v26, v9, v18
	v_mul_f32_e32 v23, v8, v19
	v_mul_f32_e32 v27, v9, v19
	v_exp_f32_e32 v20, v20
	v_exp_f32_e32 v21, v21
	v_exp_f32_e32 v22, v22
	v_exp_f32_e32 v23, v23
	v_exp_f32_e32 v24, v24
	v_exp_f32_e32 v25, v25
	v_exp_f32_e32 v26, v26
	v_exp_f32_e32 v27, v27
	v_cvt_pk_f16_f32 v58, v20, v21
	v_cvt_pk_f16_f32 v59, v22, v23
	v_cvt_pk_f16_f32 v90, v24, v25
	v_cvt_pk_f16_f32 v91, v26, v27
	v_add_f32_e32 v16, 0x42e00000, v12
	v_add_f32_e32 v17, 0x42e20000, v12
	v_add_f32_e32 v18, 0x42e40000, v12
	v_add_f32_e32 v19, 0x42e60000, v12
	v_mul_f32_e32 v16, v16, v16
	v_mul_f32_e32 v17, v17, v17
	v_mul_f32_e32 v18, v18, v18
	v_mul_f32_e32 v19, v19, v19
	v_mul_f32_e32 v20, v8, v16
	v_mul_f32_e32 v24, v9, v16
	v_mul_f32_e32 v21, v8, v17
	v_mul_f32_e32 v25, v9, v17
	v_mul_f32_e32 v22, v8, v18
	v_mul_f32_e32 v26, v9, v18
	v_mul_f32_e32 v23, v8, v19
	v_mul_f32_e32 v27, v9, v19
	v_exp_f32_e32 v20, v20
	v_exp_f32_e32 v21, v21
	v_exp_f32_e32 v22, v22
	v_exp_f32_e32 v23, v23
	v_exp_f32_e32 v24, v24
	v_exp_f32_e32 v25, v25
	v_exp_f32_e32 v26, v26
	v_exp_f32_e32 v27, v27
	v_cvt_pk_f16_f32 v60, v20, v21
	v_cvt_pk_f16_f32 v61, v22, v23
	v_cvt_pk_f16_f32 v92, v24, v25
	v_cvt_pk_f16_f32 v93, v26, v27
	v_add_f32_e32 v16, 0x42e80000, v12
	v_add_f32_e32 v17, 0x42ea0000, v12
	v_add_f32_e32 v18, 0x42ec0000, v12
	v_add_f32_e32 v19, 0x42ee0000, v12
	v_mul_f32_e32 v16, v16, v16
	v_mul_f32_e32 v17, v17, v17
	v_mul_f32_e32 v18, v18, v18
	v_mul_f32_e32 v19, v19, v19
	v_mul_f32_e32 v20, v8, v16
	v_mul_f32_e32 v24, v9, v16
	v_mul_f32_e32 v21, v8, v17
	v_mul_f32_e32 v25, v9, v17
	v_mul_f32_e32 v22, v8, v18
	v_mul_f32_e32 v26, v9, v18
	v_mul_f32_e32 v23, v8, v19
	v_mul_f32_e32 v27, v9, v19
	v_exp_f32_e32 v20, v20
	v_exp_f32_e32 v21, v21
	v_exp_f32_e32 v22, v22
	v_exp_f32_e32 v23, v23
	v_exp_f32_e32 v24, v24
	v_exp_f32_e32 v25, v25
	v_exp_f32_e32 v26, v26
	v_exp_f32_e32 v27, v27
	v_cvt_pk_f16_f32 v62, v20, v21
	v_cvt_pk_f16_f32 v63, v22, v23
	v_cvt_pk_f16_f32 v94, v24, v25
	v_cvt_pk_f16_f32 v95, v26, v27
	v_add_u32_e32 v6, 0x8000, v6
	global_load_dwordx4 v[208:211], v6, s[12:13] offset:0 nt
	global_load_dwordx4 v[212:215], v6, s[12:13] offset:1024 nt
	global_load_dwordx4 v[216:219], v6, s[12:13] offset:2048 nt
	global_load_dwordx4 v[220:223], v6, s[12:13] offset:3072 nt
	v_mul_f32_e32 v16, v13, v13
	v_add_f32_e32 v17, 0x3f800000, v13
	v_add_f32_e32 v18, 0x40000000, v13
	v_add_f32_e32 v19, 0x40400000, v13
	v_mul_f32_e32 v17, v17, v17
	v_mul_f32_e32 v18, v18, v18
	v_mul_f32_e32 v19, v19, v19
	v_mul_f32_e32 v20, v8, v16
	v_mul_f32_e32 v24, v9, v16
	v_mul_f32_e32 v21, v8, v17
	v_mul_f32_e32 v25, v9, v17
	v_mul_f32_e32 v22, v8, v18
	v_mul_f32_e32 v26, v9, v18
	v_mul_f32_e32 v23, v8, v19
	v_mul_f32_e32 v27, v9, v19
	v_exp_f32_e32 v20, v20
	v_exp_f32_e32 v21, v21
	v_exp_f32_e32 v22, v22
	v_exp_f32_e32 v23, v23
	v_exp_f32_e32 v24, v24
	v_exp_f32_e32 v25, v25
	v_exp_f32_e32 v26, v26
	v_exp_f32_e32 v27, v27
	v_mul_f32_e32 v96, v10, v20
	v_mul_f32_e32 v97, v10, v21
	v_mul_f32_e32 v98, v10, v22
	v_mul_f32_e32 v99, v10, v23
	v_mul_f32_e32 v112, v11, v24
	v_mul_f32_e32 v113, v11, v25
	v_mul_f32_e32 v114, v11, v26
	v_mul_f32_e32 v115, v11, v27
	v_add_f32_e32 v16, 0x41000000, v13
	v_add_f32_e32 v17, 0x41100000, v13
	v_add_f32_e32 v18, 0x41200000, v13
	v_add_f32_e32 v19, 0x41300000, v13
	v_mul_f32_e32 v16, v16, v16
	v_mul_f32_e32 v17, v17, v17
	v_mul_f32_e32 v18, v18, v18
	v_mul_f32_e32 v19, v19, v19
	v_mul_f32_e32 v20, v8, v16
	v_mul_f32_e32 v24, v9, v16
	v_mul_f32_e32 v21, v8, v17
	v_mul_f32_e32 v25, v9, v17
	v_mul_f32_e32 v22, v8, v18
	v_mul_f32_e32 v26, v9, v18
	v_mul_f32_e32 v23, v8, v19
	v_mul_f32_e32 v27, v9, v19
	v_exp_f32_e32 v20, v20
	v_exp_f32_e32 v21, v21
	v_exp_f32_e32 v22, v22
	v_exp_f32_e32 v23, v23
	v_exp_f32_e32 v24, v24
	v_exp_f32_e32 v25, v25
	v_exp_f32_e32 v26, v26
	v_exp_f32_e32 v27, v27
	v_mul_f32_e32 v100, v10, v20
	v_mul_f32_e32 v101, v10, v21
	v_mul_f32_e32 v102, v10, v22
	v_mul_f32_e32 v103, v10, v23
	v_mul_f32_e32 v116, v11, v24
	v_mul_f32_e32 v117, v11, v25
	v_mul_f32_e32 v118, v11, v26
	v_mul_f32_e32 v119, v11, v27
	v_add_u32_e32 v6, 0x8000, v6
	global_load_dwordx4 v[224:227], v6, s[12:13] offset:0 nt
	global_load_dwordx4 v[228:231], v6, s[12:13] offset:1024 nt
	global_load_dwordx4 v[232:235], v6, s[12:13] offset:2048 nt
	global_load_dwordx4 v[236:239], v6, s[12:13] offset:3072 nt
	v_add_f32_e32 v16, 0x41800000, v13
	v_add_f32_e32 v17, 0x41880000, v13
	v_add_f32_e32 v18, 0x41900000, v13
	v_add_f32_e32 v19, 0x41980000, v13
	v_mul_f32_e32 v16, v16, v16
	v_mul_f32_e32 v17, v17, v17
	v_mul_f32_e32 v18, v18, v18
	v_mul_f32_e32 v19, v19, v19
	v_mul_f32_e32 v20, v8, v16
	v_mul_f32_e32 v24, v9, v16
	v_mul_f32_e32 v21, v8, v17
	v_mul_f32_e32 v25, v9, v17
	v_mul_f32_e32 v22, v8, v18
	v_mul_f32_e32 v26, v9, v18
	v_mul_f32_e32 v23, v8, v19
	v_mul_f32_e32 v27, v9, v19
	v_exp_f32_e32 v20, v20
	v_exp_f32_e32 v21, v21
	v_exp_f32_e32 v22, v22
	v_exp_f32_e32 v23, v23
	v_exp_f32_e32 v24, v24
	v_exp_f32_e32 v25, v25
	v_exp_f32_e32 v26, v26
	v_exp_f32_e32 v27, v27
	v_mul_f32_e32 v104, v10, v20
	v_mul_f32_e32 v105, v10, v21
	v_mul_f32_e32 v106, v10, v22
	v_mul_f32_e32 v107, v10, v23
	v_mul_f32_e32 v120, v11, v24
	v_mul_f32_e32 v121, v11, v25
	v_mul_f32_e32 v122, v11, v26
	v_mul_f32_e32 v123, v11, v27
	v_add_f32_e32 v16, 0x41c00000, v13
	v_add_f32_e32 v17, 0x41c80000, v13
	v_add_f32_e32 v18, 0x41d00000, v13
	v_add_f32_e32 v19, 0x41d80000, v13
	v_mul_f32_e32 v16, v16, v16
	v_mul_f32_e32 v17, v17, v17
	v_mul_f32_e32 v18, v18, v18
	v_mul_f32_e32 v19, v19, v19
	v_mul_f32_e32 v20, v8, v16
	v_mul_f32_e32 v24, v9, v16
	v_mul_f32_e32 v21, v8, v17
	v_mul_f32_e32 v25, v9, v17
	v_mul_f32_e32 v22, v8, v18
	v_mul_f32_e32 v26, v9, v18
	v_mul_f32_e32 v23, v8, v19
	v_mul_f32_e32 v27, v9, v19
	v_exp_f32_e32 v20, v20
	v_exp_f32_e32 v21, v21
	v_exp_f32_e32 v22, v22
	v_exp_f32_e32 v23, v23
	v_exp_f32_e32 v24, v24
	v_exp_f32_e32 v25, v25
	v_exp_f32_e32 v26, v26
	v_exp_f32_e32 v27, v27
	v_mul_f32_e32 v108, v10, v20
	v_mul_f32_e32 v109, v10, v21
	v_mul_f32_e32 v110, v10, v22
	v_mul_f32_e32 v111, v10, v23
	v_mul_f32_e32 v124, v11, v24
	v_mul_f32_e32 v125, v11, v25
	v_mul_f32_e32 v126, v11, v26
	v_mul_f32_e32 v127, v11, v27
	v_add_u32_e32 v6, 0x8000, v6
	global_load_dwordx4 v[240:243], v6, s[12:13] offset:0 nt
	global_load_dwordx4 v[244:247], v6, s[12:13] offset:1024 nt
	global_load_dwordx4 v[248:251], v6, s[12:13] offset:2048 nt
	global_load_dwordx4 v[252:255], v6, s[12:13] offset:3072 nt
	s_waitcnt vmcnt(28)
	v_add_f32_e32 v128, v128, v129
	v_add_f32_e32 v130, v130, v131
	v_add_f32_e32 v132, v132, v133
	v_add_f32_e32 v134, v134, v135
	v_add_f32_e32 v136, v136, v137
	v_add_f32_e32 v138, v138, v139
	v_add_f32_e32 v140, v140, v141
	v_add_f32_e32 v142, v142, v143
	v_add_f32_e32 v128, v128, v130
	v_add_f32_e32 v132, v132, v134
	v_add_f32_e32 v136, v136, v138
	v_add_f32_e32 v140, v140, v142
	v_cndmask_b32_e64 v130, v128, v132, s[30:31]
	v_cndmask_b32_e64 v134, v136, v140, s[30:31]
	v_cndmask_b32_e64 v129, v132, v128, s[30:31]
	v_cndmask_b32_e64 v133, v140, v136, s[30:31]
	v_add_f32_dpp v129, v130, v129 quad_perm:[1,0,3,2] row_mask:0xf bank_mask:0xf bound_ctrl:1
	v_add_f32_dpp v133, v134, v133 quad_perm:[1,0,3,2] row_mask:0xf bank_mask:0xf bound_ctrl:1
	v_cndmask_b32_e64 v135, v129, v133, s[32:33]
	v_cndmask_b32_e64 v131, v133, v129, s[32:33]
	s_nop 1
	v_add_f32_dpp v131, v135, v131 quad_perm:[2,3,0,1] row_mask:0xf bank_mask:0xf bound_ctrl:1
	v_cvt_f16_f32_e32 v131, v131
	ds_write_b16 v14, v131 offset:0
	s_waitcnt vmcnt(24)
	v_add_f32_e32 v144, v144, v145
	v_add_f32_e32 v146, v146, v147
	v_add_f32_e32 v148, v148, v149
	v_add_f32_e32 v150, v150, v151
	v_add_f32_e32 v152, v152, v153
	v_add_f32_e32 v154, v154, v155
	v_add_f32_e32 v156, v156, v157
	v_add_f32_e32 v158, v158, v159
	v_add_f32_e32 v144, v144, v146
	v_add_f32_e32 v148, v148, v150
	v_add_f32_e32 v152, v152, v154
	v_add_f32_e32 v156, v156, v158
	v_cndmask_b32_e64 v146, v144, v148, s[30:31]
	v_cndmask_b32_e64 v150, v152, v156, s[30:31]
	v_cndmask_b32_e64 v145, v148, v144, s[30:31]
	v_cndmask_b32_e64 v149, v156, v152, s[30:31]
	v_add_f32_dpp v145, v146, v145 quad_perm:[1,0,3,2] row_mask:0xf bank_mask:0xf bound_ctrl:1
	v_add_f32_dpp v149, v150, v149 quad_perm:[1,0,3,2] row_mask:0xf bank_mask:0xf bound_ctrl:1
	v_cndmask_b32_e64 v151, v145, v149, s[32:33]
	v_cndmask_b32_e64 v147, v149, v145, s[32:33]
	s_nop 1
	v_add_f32_dpp v147, v151, v147 quad_perm:[2,3,0,1] row_mask:0xf bank_mask:0xf bound_ctrl:1
	v_cvt_f16_f32_e32 v147, v147
	ds_write_b16 v14, v147 offset:1088
	s_waitcnt vmcnt(20)
	v_add_f32_e32 v160, v160, v161
	v_add_f32_e32 v162, v162, v163
	v_add_f32_e32 v164, v164, v165
	v_add_f32_e32 v166, v166, v167
	v_add_f32_e32 v168, v168, v169
	v_add_f32_e32 v170, v170, v171
	v_add_f32_e32 v172, v172, v173
	v_add_f32_e32 v174, v174, v175
	v_add_f32_e32 v160, v160, v162
	v_add_f32_e32 v164, v164, v166
	v_add_f32_e32 v168, v168, v170
	v_add_f32_e32 v172, v172, v174
	v_cndmask_b32_e64 v162, v160, v164, s[30:31]
	v_cndmask_b32_e64 v166, v168, v172, s[30:31]
	v_cndmask_b32_e64 v161, v164, v160, s[30:31]
	v_cndmask_b32_e64 v165, v172, v168, s[30:31]
	v_add_f32_dpp v161, v162, v161 quad_perm:[1,0,3,2] row_mask:0xf bank_mask:0xf bound_ctrl:1
	v_add_f32_dpp v165, v166, v165 quad_perm:[1,0,3,2] row_mask:0xf bank_mask:0xf bound_ctrl:1
	v_cndmask_b32_e64 v167, v161, v165, s[32:33]
	v_cndmask_b32_e64 v163, v165, v161, s[32:33]
	s_nop 1
	v_add_f32_dpp v163, v167, v163 quad_perm:[2,3,0,1] row_mask:0xf bank_mask:0xf bound_ctrl:1
	v_cvt_f16_f32_e32 v163, v163
	ds_write_b16 v14, v163 offset:2176
	s_waitcnt vmcnt(16)
	v_add_f32_e32 v176, v176, v177
	v_add_f32_e32 v178, v178, v179
	v_add_f32_e32 v180, v180, v181
	v_add_f32_e32 v182, v182, v183
	v_add_f32_e32 v184, v184, v185
	v_add_f32_e32 v186, v186, v187
	v_add_f32_e32 v188, v188, v189
	v_add_f32_e32 v190, v190, v191
	v_add_f32_e32 v176, v176, v178
	v_add_f32_e32 v180, v180, v182
	v_add_f32_e32 v184, v184, v186
	v_add_f32_e32 v188, v188, v190
	v_cndmask_b32_e64 v178, v176, v180, s[30:31]
	v_cndmask_b32_e64 v182, v184, v188, s[30:31]
	v_cndmask_b32_e64 v177, v180, v176, s[30:31]
	v_cndmask_b32_e64 v181, v188, v184, s[30:31]
	v_add_f32_dpp v177, v178, v177 quad_perm:[1,0,3,2] row_mask:0xf bank_mask:0xf bound_ctrl:1
	v_add_f32_dpp v181, v182, v181 quad_perm:[1,0,3,2] row_mask:0xf bank_mask:0xf bound_ctrl:1
	v_cndmask_b32_e64 v183, v177, v181, s[32:33]
	v_cndmask_b32_e64 v179, v181, v177, s[32:33]
	s_nop 1
	v_add_f32_dpp v179, v183, v179 quad_perm:[2,3,0,1] row_mask:0xf bank_mask:0xf bound_ctrl:1
	v_cvt_f16_f32_e32 v179, v179
	ds_write_b16 v14, v179 offset:3264
	s_waitcnt vmcnt(12)
	v_add_f32_e32 v192, v192, v193
	v_add_f32_e32 v194, v194, v195
	v_add_f32_e32 v196, v196, v197
	v_add_f32_e32 v198, v198, v199
	v_add_f32_e32 v200, v200, v201
	v_add_f32_e32 v202, v202, v203
	v_add_f32_e32 v204, v204, v205
	v_add_f32_e32 v206, v206, v207
	v_add_f32_e32 v192, v192, v194
	v_add_f32_e32 v196, v196, v198
	v_add_f32_e32 v200, v200, v202
	v_add_f32_e32 v204, v204, v206
	v_cndmask_b32_e64 v194, v192, v196, s[30:31]
	v_cndmask_b32_e64 v198, v200, v204, s[30:31]
	v_cndmask_b32_e64 v193, v196, v192, s[30:31]
	v_cndmask_b32_e64 v197, v204, v200, s[30:31]
	v_add_f32_dpp v193, v194, v193 quad_perm:[1,0,3,2] row_mask:0xf bank_mask:0xf bound_ctrl:1
	v_add_f32_dpp v197, v198, v197 quad_perm:[1,0,3,2] row_mask:0xf bank_mask:0xf bound_ctrl:1
	v_cndmask_b32_e64 v199, v193, v197, s[32:33]
	v_cndmask_b32_e64 v195, v197, v193, s[32:33]
	s_nop 1
	v_add_f32_dpp v195, v199, v195 quad_perm:[2,3,0,1] row_mask:0xf bank_mask:0xf bound_ctrl:1
	v_cvt_f16_f32_e32 v195, v195
	ds_write_b16 v14, v195 offset:4352
	s_waitcnt vmcnt(8)
	v_add_f32_e32 v208, v208, v209
	v_add_f32_e32 v210, v210, v211
	v_add_f32_e32 v212, v212, v213
	v_add_f32_e32 v214, v214, v215
	v_add_f32_e32 v216, v216, v217
	v_add_f32_e32 v218, v218, v219
	v_add_f32_e32 v220, v220, v221
	v_add_f32_e32 v222, v222, v223
	v_add_f32_e32 v208, v208, v210
	v_add_f32_e32 v212, v212, v214
	v_add_f32_e32 v216, v216, v218
	v_add_f32_e32 v220, v220, v222
	v_cndmask_b32_e64 v210, v208, v212, s[30:31]
	v_cndmask_b32_e64 v214, v216, v220, s[30:31]
	v_cndmask_b32_e64 v209, v212, v208, s[30:31]
	v_cndmask_b32_e64 v213, v220, v216, s[30:31]
	v_add_f32_dpp v209, v210, v209 quad_perm:[1,0,3,2] row_mask:0xf bank_mask:0xf bound_ctrl:1
	v_add_f32_dpp v213, v214, v213 quad_perm:[1,0,3,2] row_mask:0xf bank_mask:0xf bound_ctrl:1
	v_cndmask_b32_e64 v215, v209, v213, s[32:33]
	v_cndmask_b32_e64 v211, v213, v209, s[32:33]
	s_nop 1
	v_add_f32_dpp v211, v215, v211 quad_perm:[2,3,0,1] row_mask:0xf bank_mask:0xf bound_ctrl:1
	v_cvt_f16_f32_e32 v211, v211
	ds_write_b16 v14, v211 offset:5440
	s_waitcnt vmcnt(4)
	v_add_f32_e32 v224, v224, v225
	v_add_f32_e32 v226, v226, v227
	v_add_f32_e32 v228, v228, v229
	v_add_f32_e32 v230, v230, v231
	v_add_f32_e32 v232, v232, v233
	v_add_f32_e32 v234, v234, v235
	v_add_f32_e32 v236, v236, v237
	v_add_f32_e32 v238, v238, v239
	v_add_f32_e32 v224, v224, v226
	v_add_f32_e32 v228, v228, v230
	v_add_f32_e32 v232, v232, v234
	v_add_f32_e32 v236, v236, v238
	v_cndmask_b32_e64 v226, v224, v228, s[30:31]
	v_cndmask_b32_e64 v230, v232, v236, s[30:31]
	v_cndmask_b32_e64 v225, v228, v224, s[30:31]
	v_cndmask_b32_e64 v229, v236, v232, s[30:31]
	v_add_f32_dpp v225, v226, v225 quad_perm:[1,0,3,2] row_mask:0xf bank_mask:0xf bound_ctrl:1
	v_add_f32_dpp v229, v230, v229 quad_perm:[1,0,3,2] row_mask:0xf bank_mask:0xf bound_ctrl:1
	v_cndmask_b32_e64 v231, v225, v229, s[32:33]
	v_cndmask_b32_e64 v227, v229, v225, s[32:33]
	s_nop 1
	v_add_f32_dpp v227, v231, v227 quad_perm:[2,3,0,1] row_mask:0xf bank_mask:0xf bound_ctrl:1
	v_cvt_f16_f32_e32 v227, v227
	ds_write_b16 v14, v227 offset:6528
	s_waitcnt vmcnt(0)
	v_add_f32_e32 v240, v240, v241
	v_add_f32_e32 v242, v242, v243
	v_add_f32_e32 v244, v244, v245
	v_add_f32_e32 v246, v246, v247
	v_add_f32_e32 v248, v248, v249
	v_add_f32_e32 v250, v250, v251
	v_add_f32_e32 v252, v252, v253
	v_add_f32_e32 v254, v254, v255
	v_add_f32_e32 v240, v240, v242
	v_add_f32_e32 v244, v244, v246
	v_add_f32_e32 v248, v248, v250
	v_add_f32_e32 v252, v252, v254
	v_cndmask_b32_e64 v242, v240, v244, s[30:31]
	v_cndmask_b32_e64 v246, v248, v252, s[30:31]
	v_cndmask_b32_e64 v241, v244, v240, s[30:31]
	v_cndmask_b32_e64 v245, v252, v248, s[30:31]
	v_add_f32_dpp v241, v242, v241 quad_perm:[1,0,3,2] row_mask:0xf bank_mask:0xf bound_ctrl:1
	v_add_f32_dpp v245, v246, v245 quad_perm:[1,0,3,2] row_mask:0xf bank_mask:0xf bound_ctrl:1
	v_cndmask_b32_e64 v247, v241, v245, s[32:33]
	v_cndmask_b32_e64 v243, v245, v241, s[32:33]
	s_nop 1
	v_add_f32_dpp v243, v247, v243 quad_perm:[2,3,0,1] row_mask:0xf bank_mask:0xf bound_ctrl:1
	v_cvt_f16_f32_e32 v243, v243
	ds_write_b16 v14, v243 offset:7616
	s_waitcnt lgkmcnt(0)
	s_barrier
	ds_read_b128 v[160:163], v15 offset:0
	ds_read_b128 v[164:167], v15 offset:32
	ds_read_b128 v[168:171], v15 offset:64
	ds_read_b128 v[172:175], v15 offset:96
	ds_read_b128 v[176:179], v15 offset:128
	ds_read_b128 v[180:183], v15 offset:160
	ds_read_b128 v[184:187], v15 offset:192
	ds_read_b128 v[188:191], v15 offset:224
	s_waitcnt lgkmcnt(7)
	v_mfma_f32_32x32x16_f16 v[128:143], v[160:163], v[32:35], 0
	v_mfma_f32_32x32x16_f16 v[144:159], v[160:163], v[64:67], 0
	s_waitcnt lgkmcnt(6)
	v_mfma_f32_32x32x16_f16 v[128:143], v[164:167], v[36:39], v[128:143]
	v_mfma_f32_32x32x16_f16 v[144:159], v[164:167], v[68:71], v[144:159]
	s_waitcnt lgkmcnt(5)
	v_mfma_f32_32x32x16_f16 v[128:143], v[168:171], v[40:43], v[128:143]
	v_mfma_f32_32x32x16_f16 v[144:159], v[168:171], v[72:75], v[144:159]
	s_waitcnt lgkmcnt(4)
	v_mfma_f32_32x32x16_f16 v[128:143], v[172:175], v[44:47], v[128:143]
	v_mfma_f32_32x32x16_f16 v[144:159], v[172:175], v[76:79], v[144:159]
	s_waitcnt lgkmcnt(3)
	v_mfma_f32_32x32x16_f16 v[128:143], v[176:179], v[48:51], v[128:143]
	v_mfma_f32_32x32x16_f16 v[144:159], v[176:179], v[80:83], v[144:159]
	s_waitcnt lgkmcnt(2)
	v_mfma_f32_32x32x16_f16 v[128:143], v[180:183], v[52:55], v[128:143]
	v_mfma_f32_32x32x16_f16 v[144:159], v[180:183], v[84:87], v[144:159]
	s_waitcnt lgkmcnt(1)
	v_mfma_f32_32x32x16_f16 v[128:143], v[184:187], v[56:59], v[128:143]
	v_mfma_f32_32x32x16_f16 v[144:159], v[184:187], v[88:91], v[144:159]
	s_waitcnt lgkmcnt(0)
	v_mfma_f32_32x32x16_f16 v[128:143], v[188:191], v[60:63], v[128:143]
	v_mfma_f32_32x32x16_f16 v[144:159], v[188:191], v[92:95], v[144:159]
	s_nop 15
	s_nop 3
	v_mul_f32_e32 v16, v96, v128
	v_mul_f32_e32 v17, v97, v129
	v_mul_f32_e32 v18, v98, v130
	v_mul_f32_e32 v19, v99, v131
	v_fma_f32 v16, -v112, v144, v16
	v_fma_f32 v17, -v113, v145, v17
	v_fma_f32 v18, -v114, v146, v18
	v_fma_f32 v19, -v115, v147, v19
	v_fma_f32 v16, v100, v132, v16
	v_fma_f32 v16, -v116, v148, v16
	v_fma_f32 v17, v101, v133, v17
	v_fma_f32 v17, -v117, v149, v17
	v_fma_f32 v18, v102, v134, v18
	v_fma_f32 v18, -v118, v150, v18
	v_fma_f32 v19, v103, v135, v19
	v_fma_f32 v19, -v119, v151, v19
	v_fma_f32 v16, v104, v136, v16
	v_fma_f32 v16, -v120, v152, v16
	v_fma_f32 v17, v105, v137, v17
	v_fma_f32 v17, -v121, v153, v17
	v_fma_f32 v18, v106, v138, v18
	v_fma_f32 v18, -v122, v154, v18
	v_fma_f32 v19, v107, v139, v19
	v_fma_f32 v19, -v123, v155, v19
	v_fma_f32 v16, v108, v140, v16
	v_fma_f32 v16, -v124, v156, v16
	v_fma_f32 v17, v109, v141, v17
	v_fma_f32 v17, -v125, v157, v17
	v_fma_f32 v18, v110, v142, v18
	v_fma_f32 v18, -v126, v158, v18
	v_fma_f32 v19, v111, v143, v19
	v_fma_f32 v19, -v127, v159, v19
	v_add_f32_e32 v16, v16, v17
	v_add_f32_e32 v18, v18, v19
	v_add_f32_e32 v16, v16, v18
	v_mov_b32_e32 v17, v16
	s_lshl_b32 s6, s6, 6
	s_add_i32 s6, s6, s7
	s_lshl_b32 s6, s6, 10
	v_permlane32_swap_b32_e32 v16, v17
	v_add_u32_e32 v5, s6, v5
	v_cmp_gt_u32_e32 vcc, 32, v1
	v_add_f32_e32 v16, v16, v17
	s_and_saveexec_b64 s[2:3], vcc
	s_cbranch_execz .Ldog_main_done
	global_store_dword v5, v16, s[26:27]

.Lfunc_end0:
	.size	_Z8dog_mainPKfS0_S0_S0_S0_S0_S0_Pf, .Lfunc_end0-_Z8dog_mainPKfS0_S0_S0_S0_S0_S0_Pf
	.set _Z8dog_mainPKfS0_S0_S0_S0_S0_S0_Pf.num_vgpr, 256
	.set _Z8dog_mainPKfS0_S0_S0_S0_S0_S0_Pf.num_agpr, 0
	.set _Z8dog_mainPKfS0_S0_S0_S0_S0_S0_Pf.numbered_sgpr, 96
	.set _Z8dog_mainPKfS0_S0_S0_S0_S0_S0_Pf.num_named_barrier, 0
	.set _Z8dog_mainPKfS0_S0_S0_S0_S0_S0_Pf.private_seg_size, 0
	.set _Z8dog_mainPKfS0_S0_S0_S0_S0_S0_Pf.uses_vcc, 1
	.set _Z8dog_mainPKfS0_S0_S0_S0_S0_S0_Pf.uses_flat_scratch, 0
	.set _Z8dog_mainPKfS0_S0_S0_S0_S0_S0_Pf.has_dyn_sized_stack, 0
	.set _Z8dog_mainPKfS0_S0_S0_S0_S0_S0_Pf.has_recursion, 0
	.set _Z8dog_mainPKfS0_S0_S0_S0_S0_S0_Pf.has_indirect_call, 0

amdhsa.kernels:
  - .agpr_count:     0
    .args:
      - .address_space:  global
        .offset:         0
        .size:           8
        .value_kind:     global_buffer
      - .address_space:  global
        .offset:         8
        .size:           8
        .value_kind:     global_buffer
      - .address_space:  global
        .offset:         16
        .size:           8
        .value_kind:     global_buffer
      - .address_space:  global
        .offset:         24
        .size:           8
        .value_kind:     global_buffer
      - .address_space:  global
        .offset:         32
        .size:           8
        .value_kind:     global_buffer
      - .address_space:  global
        .offset:         40
        .size:           8
        .value_kind:     global_buffer
      - .address_space:  global
        .offset:         48
        .size:           8
        .value_kind:     global_buffer
      - .actual_access:  write_only
        .address_space:  global
        .offset:         56
        .size:           8
        .value_kind:     global_buffer
    .group_segment_fixed_size: 8704
    .kernarg_segment_align: 8
    .kernarg_segment_size: 64
    .language:       OpenCL C
    .language_version:
      - 2
      - 0
    .max_flat_workgroup_size: 512
    .name:           _Z8dog_mainPKfS0_S0_S0_S0_S0_S0_Pf
    .private_segment_fixed_size: 0
    .sgpr_count:     102
    .sgpr_spill_count: 0
    .symbol:         _Z8dog_mainPKfS0_S0_S0_S0_S0_S0_Pf.kd
    .uniform_work_group_size: 1
    .uses_dynamic_stack: false
    .vgpr_count:     256
    .vgpr_spill_count: 0
    .wavefront_size: 64
  - .agpr_count:     0
    .args:
      - .actual_access:  read_only
        .address_space:  global
        .offset:         0
        .size:           8
        .value_kind:     global_buffer
      - .actual_access:  read_only
        .address_space:  global
        .offset:         8
        .size:           8
        .value_kind:     global_buffer
      - .actual_access:  write_only
        .address_space:  global
        .offset:         16
        .size:           8
        .value_kind:     global_buffer
    .group_segment_fixed_size: 0
    .kernarg_segment_align: 8
    .kernarg_segment_size: 24
    .language:       OpenCL C
    .language_version:
      - 2
      - 0
    .max_flat_workgroup_size: 256
    .name:           _Z7dog_finPKfS0_Pf
    .private_segment_fixed_size: 0
    .sgpr_count:     16
    .sgpr_spill_count: 0
    .symbol:         _Z7dog_finPKfS0_Pf.kd
    .uniform_work_group_size: 1
    .uses_dynamic_stack: false
    .vgpr_count:     16
    .vgpr_spill_count: 0
    .wavefront_size: 64
